# grid barrier release spread over 64 words (one 64-lane atomic per group-last arriver, 4 pollers per word instead of 32)
# speedup vs baseline: 1.0024x; 1.0024x over previous
.LBB0_8:
	s_or_b64 exec, exec, s[0:1]
	s_waitcnt lgkmcnt(0)
	s_barrier
	s_add_u32 s84, s54, 0x4000
	s_getreg_b32 s0, hwreg(HW_REG_XCC_ID, 0, 4)
	s_addc_u32 s85, s55, 0
	s_and_b32 s86, s0, 15
	s_and_b32 s99, s89, 63
	s_lshl_b32 s99, s99, 7
	s_add_u32 s99, s99, 0x1000
	s_lshl_b32 s99, s99, 16
	s_and_b32 s98, s89, 7
	s_lshl_b32 s98, s98, 8
	s_or_b32 s99, s99, s98
	s_add_u32 s100, s54, 0x8000
	s_addc_u32 s101, s55, 0
	s_mov_b32 s98, s33
	v_cmp_ne_u32_e64 s[0:1], 0, v0
	v_cmp_eq_u32_e64 s[78:79], 0, v0
	s_nop 0
	v_writelane_b32 v253, s0, 34
	s_nop 1
	v_writelane_b32 v253, s1, 35
	s_and_saveexec_b64 s[0:1], s[78:79]
	s_cbranch_execz .LBB0_11
	s_mov_b64 s[4:5], exec
	v_mbcnt_lo_u32_b32 v1, s4, 0
	v_mbcnt_hi_u32_b32 v1, s5, v1
	v_cmp_eq_u32_e32 vcc, 0, v1
	s_and_b64 s[2:3], exec, vcc
	s_mov_b64 exec, s[2:3]
	s_cbranch_execz .LBB0_11
	s_lshl_b32 s2, s86, 8
	s_bcnt1_i32_b64 s3, s[4:5]
	v_mov_b32_e32 v1, s2
	v_mov_b32_e32 v2, s3
	global_atomic_add v1, v2, s[84:85] offset:1024

.LBB0_230:
	v_writelane_b32 v253, s40, 46
	s_cmp_gt_i32 s81, 1
	s_cselect_b64 s[4:5], -1, 0
	v_writelane_b32 v253, s41, 47
	v_writelane_b32 v253, s42, 48
	v_writelane_b32 v253, s43, 49
	v_writelane_b32 v253, s44, 50
	v_writelane_b32 v253, s45, 51
	v_writelane_b32 v253, s46, 52
	v_writelane_b32 v253, s47, 53
	v_writelane_b32 v253, s48, 54
	v_writelane_b32 v253, s49, 55
	v_writelane_b32 v253, s50, 56
	v_writelane_b32 v253, s51, 57
	v_writelane_b32 v253, s52, 58
	v_writelane_b32 v253, s53, 59
	s_and_b64 s[0:1], s[0:1], s[4:5]
	v_writelane_b32 v253, s54, 60
	s_andn2_b64 vcc, exec, s[0:1]
	v_writelane_b32 v253, s55, 61
	s_cbranch_vccnz .LBB0_284
	s_waitcnt vmcnt(0)
	s_barrier
	s_and_saveexec_b64 s[0:1], s[78:79]
	s_cbranch_execz .LBB0_283
	v_mov_b32_e32 v1, 0x22160
	s_waitcnt vmcnt(0) lgkmcnt(0)
	ds_read_b32 v2, v1
	v_mov_b32_e32 v3, 1
	v_mov_b32_e32 v4, s99
	v_and_b32_e32 v5, 0xffff, v4
	v_lshrrev_b32_e32 v6, 16, v4
	global_atomic_add v7, v5, v3, s[100:101] sc0
	buffer_inv sc1
	v_lshrrev_b32_e32 v8, 8, v5
	v_sub_u32_e32 v8, s98, v8
	v_add_u32_e32 v8, 7, v8
	v_lshrrev_b32_e32 v8, 3, v8
	v_mov_b32_e32 v9, s98
	v_min_u32_e32 v9, 8, v9
	v_mov_b32_e32 v10, 0
	s_waitcnt lgkmcnt(0)
	v_add_u32_e32 v2, 1, v2
	ds_write_b32 v1, v2
	v_mul_lo_u32 v8, v8, v2
	v_mul_lo_u32 v9, v9, v2
	s_waitcnt vmcnt(0)
	v_add_u32_e32 v7, 1, v7
	v_cmp_eq_u32_e32 vcc, v7, v8
	s_cbranch_vccz .Lgb_poll_0
	s_mov_b64 exec, -1
	v_mbcnt_lo_u32_b32 v4, -1, 0
	v_mbcnt_hi_u32_b32 v4, -1, v4
	v_lshlrev_b32_e32 v4, 7, v4
	v_add_u32_e32 v4, 0x1000, v4
	v_mov_b32_e32 v3, 1
	global_atomic_add v4, v3, s[100:101]
	s_mov_b64 exec, 1

.LBB0_306:
	s_cmp_gt_i32 s81, 2
	s_cselect_b64 s[4:5], -1, 0
	s_and_b64 s[0:1], s[0:1], s[4:5]
	s_andn2_b64 vcc, exec, s[0:1]
	s_cbranch_vccnz .LBB0_360
	s_waitcnt vmcnt(0)
	s_waitcnt vmcnt(0)
	s_barrier
	s_and_saveexec_b64 s[0:1], s[78:79]
	s_cbranch_execz .LBB0_359
	v_mov_b32_e32 v1, 0x22160
	s_waitcnt vmcnt(0) lgkmcnt(0)
	ds_read_b32 v2, v1
	v_mov_b32_e32 v3, 1
	v_mov_b32_e32 v4, s99
	v_and_b32_e32 v5, 0xffff, v4
	v_lshrrev_b32_e32 v6, 16, v4
	global_atomic_add v7, v5, v3, s[100:101] sc0
	buffer_inv sc1
	v_lshrrev_b32_e32 v8, 8, v5
	v_sub_u32_e32 v8, s98, v8
	v_add_u32_e32 v8, 7, v8
	v_lshrrev_b32_e32 v8, 3, v8
	v_mov_b32_e32 v9, s98
	v_min_u32_e32 v9, 8, v9
	v_mov_b32_e32 v10, 0
	s_waitcnt lgkmcnt(0)
	v_add_u32_e32 v2, 1, v2
	ds_write_b32 v1, v2
	v_mul_lo_u32 v8, v8, v2
	v_mul_lo_u32 v9, v9, v2
	s_waitcnt vmcnt(0)
	v_add_u32_e32 v7, 1, v7
	v_cmp_eq_u32_e32 vcc, v7, v8
	s_cbranch_vccz .Lgb_poll_1
	s_mov_b64 exec, -1
	v_mbcnt_lo_u32_b32 v4, -1, 0
	v_mbcnt_hi_u32_b32 v4, -1, v4
	v_lshlrev_b32_e32 v4, 7, v4
	v_add_u32_e32 v4, 0x1000, v4
	v_mov_b32_e32 v3, 1
	global_atomic_add v4, v3, s[100:101]
	s_mov_b64 exec, 1

.LBB0_427:
	s_cmp_gt_i32 s81, 3
	s_cselect_b64 s[4:5], -1, 0
	s_and_b64 s[6:7], s[36:37], s[4:5]
	s_andn2_b64 vcc, exec, s[6:7]
	s_cbranch_vccnz .LBB0_481
	s_waitcnt vmcnt(0)
	s_waitcnt vmcnt(0)
	s_barrier
	s_and_saveexec_b64 s[6:7], s[78:79]
	s_cbranch_execz .LBB0_480
	v_mov_b32_e32 v1, 0x22160
	s_waitcnt vmcnt(0) lgkmcnt(0)
	ds_read_b32 v2, v1
	v_mov_b32_e32 v3, 1
	v_mov_b32_e32 v4, s99
	v_and_b32_e32 v5, 0xffff, v4
	v_lshrrev_b32_e32 v6, 16, v4
	global_atomic_add v7, v5, v3, s[100:101] sc0
	buffer_inv sc1
	v_lshrrev_b32_e32 v8, 8, v5
	v_sub_u32_e32 v8, s98, v8
	v_add_u32_e32 v8, 7, v8
	v_lshrrev_b32_e32 v8, 3, v8
	v_mov_b32_e32 v9, s98
	v_min_u32_e32 v9, 8, v9
	v_mov_b32_e32 v10, 0
	s_waitcnt lgkmcnt(0)
	v_add_u32_e32 v2, 1, v2
	ds_write_b32 v1, v2
	v_mul_lo_u32 v8, v8, v2
	v_mul_lo_u32 v9, v9, v2
	s_waitcnt vmcnt(0)
	v_add_u32_e32 v7, 1, v7
	v_cmp_eq_u32_e32 vcc, v7, v8
	s_cbranch_vccz .Lgb_chk_2
	s_mov_b64 exec, -1
	v_mbcnt_lo_u32_b32 v4, -1, 0
	v_mbcnt_hi_u32_b32 v4, -1, v4
	v_lshlrev_b32_e32 v4, 7, v4
	v_add_u32_e32 v4, 0x1000, v4
	v_mov_b32_e32 v3, 1
	global_atomic_add v4, v3, s[100:101]
	s_mov_b64 exec, 1

.Lgw_end_2:
	v_mov_b32_e32 v7, 0x22160
	s_waitcnt vmcnt(0) lgkmcnt(0)
	ds_read_b32 v8, v7
	v_mov_b32_e32 v9, 1
	v_mov_b32_e32 v10, s99
	v_and_b32_e32 v11, 0xffff, v10
	v_lshrrev_b32_e32 v12, 16, v10
	global_atomic_add v13, v11, v9, s[100:101] sc0
	buffer_inv sc1
	v_lshrrev_b32_e32 v14, 8, v11
	v_sub_u32_e32 v14, s98, v14
	v_add_u32_e32 v14, 7, v14
	v_lshrrev_b32_e32 v14, 3, v14
	v_mov_b32_e32 v15, s98
	v_min_u32_e32 v15, 8, v15
	v_mov_b32_e32 v16, 0
	s_waitcnt lgkmcnt(0)
	v_add_u32_e32 v8, 1, v8
	ds_write_b32 v7, v8
	v_mul_lo_u32 v14, v14, v8
	v_mul_lo_u32 v15, v15, v8
	s_waitcnt vmcnt(0)
	v_add_u32_e32 v13, 1, v13
	v_cmp_eq_u32_e32 vcc, v13, v14
	s_cbranch_vccz .Lgb_done_3
	s_mov_b64 exec, -1
	v_mbcnt_lo_u32_b32 v10, -1, 0
	v_mbcnt_hi_u32_b32 v10, -1, v10
	v_lshlrev_b32_e32 v10, 7, v10
	v_add_u32_e32 v10, 0x1000, v10
	v_mov_b32_e32 v9, 1
	global_atomic_add v10, v9, s[100:101]
	s_mov_b64 exec, 1

.LBB0_759:
	s_cmp_gt_i32 s81, 4
	s_cselect_b64 s[0:1], -1, 0
	s_and_b64 s[4:5], s[4:5], s[0:1]
	s_andn2_b64 vcc, exec, s[4:5]
	s_cbranch_vccnz .LBB0_813
	s_waitcnt vmcnt(0)
	s_waitcnt vmcnt(0)
	s_barrier
	s_and_saveexec_b64 s[4:5], s[78:79]
	s_cbranch_execz .LBB0_812
	v_mov_b32_e32 v1, 0x22160
	s_waitcnt vmcnt(0) lgkmcnt(0)
	ds_read_b32 v2, v1
	v_mov_b32_e32 v3, 1
	v_mov_b32_e32 v4, s99
	v_and_b32_e32 v5, 0xffff, v4
	v_lshrrev_b32_e32 v6, 16, v4
	global_atomic_add v7, v5, v3, s[100:101] sc0
	buffer_inv sc1
	v_lshrrev_b32_e32 v8, 8, v5
	v_sub_u32_e32 v8, s98, v8
	v_add_u32_e32 v8, 7, v8
	v_lshrrev_b32_e32 v8, 3, v8
	v_mov_b32_e32 v9, s98
	v_min_u32_e32 v9, 8, v9
	v_mov_b32_e32 v10, 0
	s_waitcnt lgkmcnt(0)
	v_add_u32_e32 v2, 1, v2
	ds_write_b32 v1, v2
	v_mul_lo_u32 v8, v8, v2
	v_mul_lo_u32 v9, v9, v2
	s_waitcnt vmcnt(0)
	v_add_u32_e32 v7, 1, v7
	v_cmp_eq_u32_e32 vcc, v7, v8
	s_cbranch_vccz .Lgb_chk_4
	s_mov_b64 exec, -1
	v_mbcnt_lo_u32_b32 v4, -1, 0
	v_mbcnt_hi_u32_b32 v4, -1, v4
	v_lshlrev_b32_e32 v4, 7, v4
	v_add_u32_e32 v4, 0x1000, v4
	v_mov_b32_e32 v3, 1
	global_atomic_add v4, v3, s[100:101]
	s_mov_b64 exec, 1

.LBB0_843:
	s_cmp_gt_i32 s81, 5
	s_cselect_b64 s[4:5], -1, 0
	s_and_b64 s[0:1], s[0:1], s[4:5]
	s_andn2_b64 vcc, exec, s[0:1]
	s_cbranch_vccnz .LBB0_897
	s_waitcnt vmcnt(0)
	s_waitcnt vmcnt(0)
	s_barrier
	s_and_saveexec_b64 s[0:1], s[78:79]
	s_cbranch_execz .LBB0_896
	v_mov_b32_e32 v1, 0x22160
	s_waitcnt vmcnt(0) lgkmcnt(0)
	ds_read_b32 v2, v1
	v_mov_b32_e32 v3, 1
	v_mov_b32_e32 v4, s99
	v_and_b32_e32 v5, 0xffff, v4
	v_lshrrev_b32_e32 v6, 16, v4
	global_atomic_add v7, v5, v3, s[100:101] sc0
	buffer_inv sc1
	v_lshrrev_b32_e32 v8, 8, v5
	v_sub_u32_e32 v8, s98, v8
	v_add_u32_e32 v8, 7, v8
	v_lshrrev_b32_e32 v8, 3, v8
	v_mov_b32_e32 v9, s98
	v_min_u32_e32 v9, 8, v9
	v_mov_b32_e32 v10, 0
	s_waitcnt lgkmcnt(0)
	v_add_u32_e32 v2, 1, v2
	ds_write_b32 v1, v2
	v_mul_lo_u32 v8, v8, v2
	v_mul_lo_u32 v9, v9, v2
	s_waitcnt vmcnt(0)
	v_add_u32_e32 v7, 1, v7
	v_cmp_eq_u32_e32 vcc, v7, v8
	s_cbranch_vccz .Lgb_done_5
	s_mov_b64 exec, -1
	v_mbcnt_lo_u32_b32 v4, -1, 0
	v_mbcnt_hi_u32_b32 v4, -1, v4
	v_lshlrev_b32_e32 v4, 7, v4
	v_add_u32_e32 v4, 0x1000, v4
	v_mov_b32_e32 v3, 1
	global_atomic_add v4, v3, s[100:101]
	s_mov_b64 exec, 1

.LBB0_944:
	s_cmp_gt_i32 s81, 6
	s_cselect_b64 s[4:5], -1, 0
	s_and_b64 s[0:1], s[0:1], s[4:5]
	s_andn2_b64 vcc, exec, s[0:1]
	s_cbranch_vccnz .LBB0_998
	s_waitcnt vmcnt(0)
	s_waitcnt vmcnt(0)
	s_barrier
	s_and_saveexec_b64 s[0:1], s[78:79]
	s_cbranch_execz .LBB0_997
	v_mov_b32_e32 v1, 0x22160
	s_waitcnt vmcnt(0) lgkmcnt(0)
	ds_read_b32 v2, v1
	v_mov_b32_e32 v3, 1
	v_mov_b32_e32 v4, s99
	v_and_b32_e32 v5, 0xffff, v4
	v_lshrrev_b32_e32 v6, 16, v4
	global_atomic_add v7, v5, v3, s[100:101] sc0
	buffer_inv sc1
	v_lshrrev_b32_e32 v8, 8, v5
	v_sub_u32_e32 v8, s98, v8
	v_add_u32_e32 v8, 7, v8
	v_lshrrev_b32_e32 v8, 3, v8
	v_mov_b32_e32 v9, s98
	v_min_u32_e32 v9, 8, v9
	v_mov_b32_e32 v10, 0
	s_waitcnt lgkmcnt(0)
	v_add_u32_e32 v2, 1, v2
	ds_write_b32 v1, v2
	v_mul_lo_u32 v8, v8, v2
	v_mul_lo_u32 v9, v9, v2
	s_waitcnt vmcnt(0)
	v_add_u32_e32 v7, 1, v7
	v_cmp_eq_u32_e32 vcc, v7, v8
	s_cbranch_vccz .Lgb_poll_6
	s_mov_b64 exec, -1
	v_mbcnt_lo_u32_b32 v4, -1, 0
	v_mbcnt_hi_u32_b32 v4, -1, v4
	v_lshlrev_b32_e32 v4, 7, v4
	v_add_u32_e32 v4, 0x1000, v4
	v_mov_b32_e32 v3, 1
	global_atomic_add v4, v3, s[100:101]
	s_mov_b64 exec, 1

.Lcv_skip:
	s_cmp_gt_i32 s81, 7
	s_cselect_b64 s[4:5], -1, 0
	s_and_b64 s[0:1], s[76:77], s[4:5]
	v_readlane_b32 s86, v253, 40
	s_andn2_b64 vcc, exec, s[0:1]
	v_readlane_b32 s76, v253, 62
	v_readlane_b32 s77, v253, 63
	v_readlane_b32 s87, v253, 41
	s_cbranch_vccnz .LBB0_1205
	s_waitcnt vmcnt(0)
	s_waitcnt vmcnt(0) lgkmcnt(0)
	s_barrier
	s_and_saveexec_b64 s[0:1], s[78:79]
	s_cbranch_execz .LBB0_1204
	v_mov_b32_e32 v1, 0x22160
	s_waitcnt vmcnt(0) lgkmcnt(0)
	ds_read_b32 v2, v1
	v_mov_b32_e32 v3, 1
	v_mov_b32_e32 v4, s99
	v_and_b32_e32 v5, 0xffff, v4
	v_lshrrev_b32_e32 v6, 16, v4
	global_atomic_add v7, v5, v3, s[100:101] sc0
	buffer_inv sc1
	v_lshrrev_b32_e32 v8, 8, v5
	v_sub_u32_e32 v8, s98, v8
	v_add_u32_e32 v8, 7, v8
	v_lshrrev_b32_e32 v8, 3, v8
	v_mov_b32_e32 v9, s98
	v_min_u32_e32 v9, 8, v9
	v_mov_b32_e32 v10, 0
	s_waitcnt lgkmcnt(0)
	v_add_u32_e32 v2, 1, v2
	ds_write_b32 v1, v2
	v_mul_lo_u32 v8, v8, v2
	v_mul_lo_u32 v9, v9, v2
	s_waitcnt vmcnt(0)
	v_add_u32_e32 v7, 1, v7
	v_cmp_eq_u32_e32 vcc, v7, v8
	s_cbranch_vccz .Lgb_done_7
	s_mov_b64 exec, -1
	v_mbcnt_lo_u32_b32 v4, -1, 0
	v_mbcnt_hi_u32_b32 v4, -1, v4
	v_lshlrev_b32_e32 v4, 7, v4
	v_add_u32_e32 v4, 0x1000, v4
	v_mov_b32_e32 v3, 1
	global_atomic_add v4, v3, s[100:101]
	s_mov_b64 exec, 1

.LBB0_1220:
	s_cmp_gt_i32 s81, 8
	s_cselect_b64 s[14:15], -1, 0
	s_and_b64 s[4:5], s[12:13], s[14:15]
	s_andn2_b64 vcc, exec, s[4:5]
	s_cbranch_vccnz .LBB0_1274
	s_waitcnt vmcnt(0)
	s_waitcnt vmcnt(0) lgkmcnt(0)
	s_barrier
	s_and_saveexec_b64 s[4:5], s[78:79]
	s_cbranch_execz .LBB0_1273
	v_mov_b32_e32 v1, 0x22160
	s_waitcnt vmcnt(0) lgkmcnt(0)
	ds_read_b32 v2, v1
	v_mov_b32_e32 v3, 1
	v_mov_b32_e32 v4, s99
	v_and_b32_e32 v5, 0xffff, v4
	v_lshrrev_b32_e32 v6, 16, v4
	global_atomic_add v7, v5, v3, s[100:101] sc0
	buffer_inv sc1
	v_lshrrev_b32_e32 v8, 8, v5
	v_sub_u32_e32 v8, s98, v8
	v_add_u32_e32 v8, 7, v8
	v_lshrrev_b32_e32 v8, 3, v8
	v_mov_b32_e32 v9, s98
	v_min_u32_e32 v9, 8, v9
	v_mov_b32_e32 v10, 0
	s_waitcnt lgkmcnt(0)
	v_add_u32_e32 v2, 1, v2
	ds_write_b32 v1, v2
	v_mul_lo_u32 v8, v8, v2
	v_mul_lo_u32 v9, v9, v2
	s_waitcnt vmcnt(0)
	v_add_u32_e32 v7, 1, v7
	v_cmp_eq_u32_e32 vcc, v7, v8
	s_cbranch_vccz .Lgb_poll_8
	s_mov_b64 exec, -1
	v_mbcnt_lo_u32_b32 v4, -1, 0
	v_mbcnt_hi_u32_b32 v4, -1, v4
	v_lshlrev_b32_e32 v4, 7, v4
	v_add_u32_e32 v4, 0x1000, v4
	v_mov_b32_e32 v3, 1
	global_atomic_add v4, v3, s[100:101]
	s_mov_b64 exec, 1

.LBB0_1606:
	s_cmp_gt_i32 s81, 10
	s_cselect_b64 s[0:1], -1, 0
	s_and_b64 s[4:5], s[12:13], s[0:1]
	s_andn2_b64 vcc, exec, s[4:5]
	s_waitcnt vmcnt(0)
	v_and_b32_e32 v82, 63, v0
	s_cbranch_vccnz .LBB0_1660
	s_waitcnt vmcnt(0)
	s_waitcnt lgkmcnt(0)
	s_barrier
	s_and_saveexec_b64 s[4:5], s[78:79]
	s_cbranch_execz .LBB0_1659
	v_mov_b32_e32 v1, 0x22160
	s_waitcnt vmcnt(0) lgkmcnt(0)
	ds_read_b32 v2, v1
	v_mov_b32_e32 v3, 1
	v_mov_b32_e32 v4, s99
	v_and_b32_e32 v5, 0xffff, v4
	v_lshrrev_b32_e32 v6, 16, v4
	global_atomic_add v7, v5, v3, s[100:101] sc0
	buffer_inv sc1
	v_mov_b32_e32 v12, 0
	global_load_dword v11, v12, s[100:101] offset:128 sc1
	v_lshrrev_b32_e32 v8, 8, v5
	v_sub_u32_e32 v8, s98, v8
	v_add_u32_e32 v8, 7, v8
	v_lshrrev_b32_e32 v8, 3, v8
	v_mov_b32_e32 v9, s98
	v_min_u32_e32 v9, 8, v9
	v_mov_b32_e32 v10, 0
	s_waitcnt lgkmcnt(0)
	v_add_u32_e32 v2, 1, v2
	ds_write_b32 v1, v2
	v_mul_lo_u32 v8, v8, v2
	v_mul_lo_u32 v9, v9, v2
	s_waitcnt vmcnt(0)
	v_add_u32_e32 v7, 1, v7
	v_cmp_eq_u32_e32 vcc, v7, v8
	s_cbranch_vccz .Lgb_chk_9
	s_mov_b64 exec, -1
	v_mbcnt_lo_u32_b32 v4, -1, 0
	v_mbcnt_hi_u32_b32 v4, -1, v4
	v_lshlrev_b32_e32 v4, 7, v4
	v_add_u32_e32 v4, 0x1000, v4
	v_mov_b32_e32 v3, 1
	global_atomic_add v4, v3, s[100:101]
	s_mov_b64 exec, 1

.LBB0_1750:
	s_waitcnt vmcnt(0)
	s_waitcnt lgkmcnt(0)
	s_barrier
	s_mov_b64 s[6:7], exec
	v_readlane_b32 s40, v253, 46
	s_and_b64 s[8:9], s[6:7], s[78:79]
	v_readlane_b32 s41, v253, 47
	v_readlane_b32 s42, v253, 48
	v_readlane_b32 s43, v253, 49
	v_readlane_b32 s44, v253, 50
	v_readlane_b32 s45, v253, 51
	v_readlane_b32 s52, v253, 58
	v_readlane_b32 s53, v253, 59
	v_readlane_b32 s54, v253, 60
	v_readlane_b32 s55, v253, 61
	v_and_b32_e32 v82, 63, v0
	v_readlane_b32 s46, v253, 52
	v_readlane_b32 s47, v253, 53
	v_readlane_b32 s48, v253, 54
	v_readlane_b32 s49, v253, 55
	v_readlane_b32 s50, v253, 56
	v_readlane_b32 s51, v253, 57
	s_mov_b64 exec, s[8:9]
	s_cbranch_execz .LBB0_1802
	v_mov_b32_e32 v2, 0x22160
	s_waitcnt vmcnt(0) lgkmcnt(0)
	ds_read_b32 v3, v2
	v_mov_b32_e32 v4, 1
	v_mov_b32_e32 v5, s99
	v_and_b32_e32 v6, 0xffff, v5
	v_lshrrev_b32_e32 v7, 16, v5
	global_atomic_add v8, v6, v4, s[100:101] sc0
	buffer_inv sc1
	v_lshrrev_b32_e32 v9, 8, v6
	v_sub_u32_e32 v9, s98, v9
	v_add_u32_e32 v9, 7, v9
	v_lshrrev_b32_e32 v9, 3, v9
	v_mov_b32_e32 v10, s98
	v_min_u32_e32 v10, 8, v10
	v_mov_b32_e32 v11, 0
	s_waitcnt lgkmcnt(0)
	v_add_u32_e32 v3, 1, v3
	ds_write_b32 v2, v3
	v_mul_lo_u32 v9, v9, v3
	v_mul_lo_u32 v10, v10, v3
	s_waitcnt vmcnt(0)
	v_add_u32_e32 v8, 1, v8
	v_cmp_eq_u32_e32 vcc, v8, v9
	s_cbranch_vccz .Lgb_poll_10
	s_mov_b64 exec, -1
	v_mbcnt_lo_u32_b32 v5, -1, 0
	v_mbcnt_hi_u32_b32 v5, -1, v5
	v_lshlrev_b32_e32 v5, 7, v5
	v_add_u32_e32 v5, 0x1000, v5
	v_mov_b32_e32 v4, 1
	global_atomic_add v5, v4, s[100:101]
	s_mov_b64 exec, 1

.LBB0_1811:
	s_cmp_gt_i32 s81, 11
	s_cselect_b64 s[4:5], -1, 0
	s_and_b64 s[0:1], s[0:1], s[4:5]
	v_readlane_b32 s36, v253, 46
	s_andn2_b64 vcc, exec, s[0:1]
	v_readlane_b32 s37, v253, 47
	v_readlane_b32 s38, v253, 48
	v_readlane_b32 s39, v253, 49
	v_readlane_b32 s40, v253, 50
	v_readlane_b32 s41, v253, 51
	v_readlane_b32 s48, v253, 58
	v_readlane_b32 s49, v253, 59
	v_readlane_b32 s50, v253, 60
	v_readlane_b32 s51, v253, 61
	v_readlane_b32 s42, v253, 52
	v_readlane_b32 s43, v253, 53
	v_readlane_b32 s44, v253, 54
	v_readlane_b32 s45, v253, 55
	v_readlane_b32 s46, v253, 56
	v_readlane_b32 s47, v253, 57
	s_cbranch_vccnz .LBB0_1865
	s_waitcnt vmcnt(0)
	s_waitcnt lgkmcnt(0)
	s_barrier
	s_and_saveexec_b64 s[0:1], s[78:79]
	s_cbranch_execz .LBB0_1864
	v_mov_b32_e32 v1, 0x22160
	s_waitcnt vmcnt(0) lgkmcnt(0)
	ds_read_b32 v2, v1
	v_mov_b32_e32 v3, 1
	v_mov_b32_e32 v4, s99
	v_and_b32_e32 v5, 0xffff, v4
	v_lshrrev_b32_e32 v6, 16, v4
	global_atomic_add v7, v5, v3, s[100:101] sc0
	buffer_inv sc1
	v_lshrrev_b32_e32 v8, 8, v5
	v_sub_u32_e32 v8, s98, v8
	v_add_u32_e32 v8, 7, v8
	v_lshrrev_b32_e32 v8, 3, v8
	v_mov_b32_e32 v9, s98
	v_min_u32_e32 v9, 8, v9
	v_mov_b32_e32 v10, 0
	s_waitcnt lgkmcnt(0)
	v_add_u32_e32 v2, 1, v2
	ds_write_b32 v1, v2
	v_mul_lo_u32 v8, v8, v2
	v_mul_lo_u32 v9, v9, v2
	s_waitcnt vmcnt(0)
	v_add_u32_e32 v7, 1, v7
	v_cmp_eq_u32_e32 vcc, v7, v8
	s_cbranch_vccz .Lgb_poll_11
	s_mov_b64 exec, -1
	v_mbcnt_lo_u32_b32 v4, -1, 0
	v_mbcnt_hi_u32_b32 v4, -1, v4
	v_lshlrev_b32_e32 v4, 7, v4
	v_add_u32_e32 v4, 0x1000, v4
	v_mov_b32_e32 v3, 1
	global_atomic_add v4, v3, s[100:101]
	s_mov_b64 exec, 1

.LBB0_1890:
	s_cmp_gt_i32 s81, 12
	s_cselect_b64 s[2:3], -1, 0
	s_and_b64 s[0:1], s[0:1], s[2:3]
	s_andn2_b64 vcc, exec, s[0:1]
	s_cbranch_vccnz .LBB0_1944
	s_waitcnt vmcnt(0)
	s_waitcnt lgkmcnt(0)
	s_barrier
	s_and_saveexec_b64 s[0:1], s[78:79]
	s_cbranch_execz .LBB0_1943
	v_mov_b32_e32 v1, 0x22160
	s_waitcnt vmcnt(0) lgkmcnt(0)
	ds_read_b32 v2, v1
	v_mov_b32_e32 v3, 1
	v_mov_b32_e32 v4, s99
	v_and_b32_e32 v5, 0xffff, v4
	v_lshrrev_b32_e32 v6, 16, v4
	global_atomic_add v7, v5, v3, s[100:101] sc0
	buffer_inv sc1
	v_lshrrev_b32_e32 v8, 8, v5
	v_sub_u32_e32 v8, s98, v8
	v_add_u32_e32 v8, 7, v8
	v_lshrrev_b32_e32 v8, 3, v8
	v_mov_b32_e32 v9, s98
	v_min_u32_e32 v9, 8, v9
	v_mov_b32_e32 v10, 0
	s_waitcnt lgkmcnt(0)
	v_add_u32_e32 v2, 1, v2
	ds_write_b32 v1, v2
	v_mul_lo_u32 v8, v8, v2
	v_mul_lo_u32 v9, v9, v2
	s_waitcnt vmcnt(0)
	v_add_u32_e32 v7, 1, v7
	v_cmp_eq_u32_e32 vcc, v7, v8
	s_cbranch_vccz .Lgb_done_12
	s_mov_b64 exec, -1
	v_mbcnt_lo_u32_b32 v4, -1, 0
	v_mbcnt_hi_u32_b32 v4, -1, v4
	v_lshlrev_b32_e32 v4, 7, v4
	v_add_u32_e32 v4, 0x1000, v4
	v_mov_b32_e32 v3, 1
	global_atomic_add v4, v3, s[100:101]
	s_mov_b64 exec, 1

.LBB0_1991:
	s_cmp_gt_i32 s81, 13
	s_cselect_b64 s[2:3], -1, 0
	s_and_b64 s[0:1], s[0:1], s[2:3]
	s_andn2_b64 vcc, exec, s[0:1]
	s_cbranch_vccnz .LBB0_2045
	s_waitcnt vmcnt(0)
	s_waitcnt lgkmcnt(0)
	s_barrier
	s_and_saveexec_b64 s[0:1], s[78:79]
	s_cbranch_execz .LBB0_2044
	v_mov_b32_e32 v1, 0x22160
	s_waitcnt vmcnt(0) lgkmcnt(0)
	ds_read_b32 v2, v1
	v_mov_b32_e32 v3, 1
	v_mov_b32_e32 v4, s99
	v_and_b32_e32 v5, 0xffff, v4
	v_lshrrev_b32_e32 v6, 16, v4
	global_atomic_add v7, v5, v3, s[100:101] sc0
	buffer_inv sc1
	v_lshrrev_b32_e32 v8, 8, v5
	v_sub_u32_e32 v8, s98, v8
	v_add_u32_e32 v8, 7, v8
	v_lshrrev_b32_e32 v8, 3, v8
	v_mov_b32_e32 v9, s98
	v_min_u32_e32 v9, 8, v9
	v_mov_b32_e32 v10, 0
	s_waitcnt lgkmcnt(0)
	v_add_u32_e32 v2, 1, v2
	ds_write_b32 v1, v2
	v_mul_lo_u32 v8, v8, v2
	v_mul_lo_u32 v9, v9, v2
	s_waitcnt vmcnt(0)
	v_add_u32_e32 v7, 1, v7
	v_cmp_eq_u32_e32 vcc, v7, v8
	s_cbranch_vccz .Lgb_poll_13
	s_mov_b64 exec, -1
	v_mbcnt_lo_u32_b32 v4, -1, 0
	v_mbcnt_hi_u32_b32 v4, -1, v4
	v_lshlrev_b32_e32 v4, 7, v4
	v_add_u32_e32 v4, 0x1000, v4
	v_mov_b32_e32 v3, 1
	global_atomic_add v4, v3, s[100:101]
	s_mov_b64 exec, 1
